# v43 with the barrier leader's write-back issued before its invalidate and the poll loop without s_sleep
# speedup vs baseline: 1.0095x; 1.0025x over previous
; __device__ __forceinline__ unsigned xb_ld(unsigned* p)              { return __hip_atomic_load(p, __ATOMIC_RELAXED, __HIP_MEMORY_SCOPE_AGENT); }
; __device__ __forceinline__ unsigned xb_add(unsigned* p, unsigned v) { return __hip_atomic_fetch_add(p, v, __ATOMIC_RELAXED, __HIP_MEMORY_SCOPE_AGENT); }
; #define XB_SPIN(cond, bar) do { unsigned _sp = 0; while (cond) { __builtin_amdgcn_s_sleep(1); \
;     if ((++_sp & 255u) == 0u) { if (xb_ld(&(bar)[XB_TMO])) break; if (_sp > XB_SPIN_CAP) { atomicAdd(&(bar)[XB_TMO], 1u); break; } } } } while (0)
; __device__ __forceinline__ void xcd_barrier(const XcdBarrier& b) {
;     asm volatile("s_waitcnt vmcnt(0)" ::: "memory");
;     __syncthreads();
;     if (threadIdx.x == 0) {
;         unsigned* bar = b.bar;
;         __builtin_amdgcn_s_waitcnt(0);
;         unsigned nloc = b.st[0], nx = b.st[1];
;         if (nloc == 0u) { xcd_barrier_complete(bar, b.x, nloc, nx); b.st[0] = nloc; b.st[1] = nx; }
;         const unsigned old = xb_add(&bar[XB_XSUB(b.x)], 1u);
;         const unsigned gen = old / nloc;
;         if (old + 1u == (gen + 1u) * nloc) {
;             __builtin_amdgcn_fence(__ATOMIC_RELEASE, "agent");
;             asm volatile("s_waitcnt vmcnt(0)" ::: "memory");
;             const unsigned og = xb_add(&bar[XB_TOP], 1u);
;             const unsigned tg = og / nx;
;             if (og + 1u == (tg + 1u) * nx) xb_add(&bar[XB_TOPGEN], 1u);
;             else XB_SPIN(xb_ld(&bar[XB_TOPGEN]) == tg, bar);
;             __builtin_amdgcn_fence(__ATOMIC_ACQUIRE, "agent");
;             xb_add(&bar[XB_XGEN(b.x)], 1u);
;             asm volatile("s_waitcnt vmcnt(0)" ::: "memory");
;         } else {
;             XB_SPIN(xb_ld(&bar[XB_XGEN(b.x)]) == gen, bar);
;             __builtin_amdgcn_fence(__ATOMIC_ACQUIRE, "agent");
;             asm volatile("s_waitcnt vmcnt(0)" ::: "memory");
;         }
.LBB0_228:
	s_waitcnt lgkmcnt(0)
	v_readfirstlane_b32 s8, v3
	v_readfirstlane_b32 s9, v1
	v_readlane_b32 s0, v252, 4
	s_lshl_b32 s0, s0, 8
	v_readlane_b32 s2, v252, 2
	v_readlane_b32 s3, v252, 3
	s_add_u32 s6, s2, s0
	s_addc_u32 s7, s3, 0
	s_mul_i32 s10, s8, 1
	s_mul_i32 s11, s9, 1
	v_mov_b32_e32 v4, 0x1000
	v_mov_b32_e32 v5, 1
	global_atomic_add v4, v4, v5, s[6:7] offset:1024 sc0
	v_mov_b32_e32 v1, 0x3400
	s_waitcnt vmcnt(0)
	v_readfirstlane_b32 s0, v4
	s_add_u32 s0, s0, 1
	s_cmp_lg_u32 s0, s10
	s_cbranch_scc1 .Lgbn_0
	buffer_wbl2 sc1
	buffer_inv sc1
	s_waitcnt vmcnt(0)
	global_atomic_add v1, v5, s[2:3]
	s_branch .Lgbw_0
.Lgbn_0:
	buffer_inv sc1

; __device__ __forceinline__ unsigned xb_ld(unsigned* p)              { return __hip_atomic_load(p, __ATOMIC_RELAXED, __HIP_MEMORY_SCOPE_AGENT); }
; __device__ __forceinline__ unsigned xb_add(unsigned* p, unsigned v) { return __hip_atomic_fetch_add(p, v, __ATOMIC_RELAXED, __HIP_MEMORY_SCOPE_AGENT); }
; #define XB_SPIN(cond, bar) do { unsigned _sp = 0; while (cond) { __builtin_amdgcn_s_sleep(1); \
;     if ((++_sp & 255u) == 0u) { if (xb_ld(&(bar)[XB_TMO])) break; if (_sp > XB_SPIN_CAP) { atomicAdd(&(bar)[XB_TMO], 1u); break; } } } } while (0)
; __device__ __forceinline__ void xcd_barrier(const XcdBarrier& b) {
;     ...
;             else XB_SPIN(xb_ld(&bar[XB_TOPGEN]) == tg, bar);
;             __builtin_amdgcn_fence(__ATOMIC_ACQUIRE, "agent");
;             xb_add(&bar[XB_XGEN(b.x)], 1u);
;             asm volatile("s_waitcnt vmcnt(0)" ::: "memory");
;         } else {
;             XB_SPIN(xb_ld(&bar[XB_XGEN(b.x)]) == gen, bar);
.Lgbs_0:
	global_load_dword v2, v1, s[2:3] sc1
	s_waitcnt vmcnt(0)
	v_readfirstlane_b32 s0, v2
	s_cmp_ge_u32 s0, s11
	s_cbranch_scc1 .Lgbd_0
	s_add_u32 s1, s1, 1
	s_cmp_lt_u32 s1, 0x40000
	s_cbranch_scc1 .Lgbs_0

; __device__ __forceinline__ unsigned xb_ld(unsigned* p)              { return __hip_atomic_load(p, __ATOMIC_RELAXED, __HIP_MEMORY_SCOPE_AGENT); }
; __device__ __forceinline__ unsigned xb_add(unsigned* p, unsigned v) { return __hip_atomic_fetch_add(p, v, __ATOMIC_RELAXED, __HIP_MEMORY_SCOPE_AGENT); }
; #define XB_SPIN(cond, bar) do { unsigned _sp = 0; while (cond) { __builtin_amdgcn_s_sleep(1); \
;     if ((++_sp & 255u) == 0u) { if (xb_ld(&(bar)[XB_TMO])) break; if (_sp > XB_SPIN_CAP) { atomicAdd(&(bar)[XB_TMO], 1u); break; } } } } while (0)
; __device__ __forceinline__ void xcd_barrier(const XcdBarrier& b) {
;     asm volatile("s_waitcnt vmcnt(0)" ::: "memory");
;     __syncthreads();
;     if (threadIdx.x == 0) {
;         unsigned* bar = b.bar;
;         __builtin_amdgcn_s_waitcnt(0);
;         unsigned nloc = b.st[0], nx = b.st[1];
;         if (nloc == 0u) { xcd_barrier_complete(bar, b.x, nloc, nx); b.st[0] = nloc; b.st[1] = nx; }
;         const unsigned old = xb_add(&bar[XB_XSUB(b.x)], 1u);
;         const unsigned gen = old / nloc;
;         if (old + 1u == (gen + 1u) * nloc) {
;             __builtin_amdgcn_fence(__ATOMIC_RELEASE, "agent");
;             asm volatile("s_waitcnt vmcnt(0)" ::: "memory");
;             const unsigned og = xb_add(&bar[XB_TOP], 1u);
;             const unsigned tg = og / nx;
;             if (og + 1u == (tg + 1u) * nx) xb_add(&bar[XB_TOPGEN], 1u);
;             else XB_SPIN(xb_ld(&bar[XB_TOPGEN]) == tg, bar);
;             __builtin_amdgcn_fence(__ATOMIC_ACQUIRE, "agent");
;             xb_add(&bar[XB_XGEN(b.x)], 1u);
;             asm volatile("s_waitcnt vmcnt(0)" ::: "memory");
;         } else {
;             XB_SPIN(xb_ld(&bar[XB_XGEN(b.x)]) == gen, bar);
;             __builtin_amdgcn_fence(__ATOMIC_ACQUIRE, "agent");
;             asm volatile("s_waitcnt vmcnt(0)" ::: "memory");
;         }
.LBB0_312:
	s_waitcnt lgkmcnt(0)
	v_readfirstlane_b32 s8, v3
	v_readfirstlane_b32 s9, v1
	v_readlane_b32 s0, v252, 4
	s_lshl_b32 s0, s0, 8
	v_readlane_b32 s2, v252, 2
	v_readlane_b32 s3, v252, 3
	s_add_u32 s6, s2, s0
	s_addc_u32 s7, s3, 0
	s_mul_i32 s10, s8, 2
	s_mul_i32 s11, s9, 2
	v_mov_b32_e32 v4, 0x1000
	v_mov_b32_e32 v5, 1
	global_atomic_add v4, v4, v5, s[6:7] offset:1024 sc0
	v_mov_b32_e32 v1, 0x3400
	s_waitcnt vmcnt(0)
	v_readfirstlane_b32 s0, v4
	s_add_u32 s0, s0, 1
	s_cmp_lg_u32 s0, s10
	s_cbranch_scc1 .Lgbn_1
	buffer_wbl2 sc1
	buffer_inv sc1
	s_waitcnt vmcnt(0)
	global_atomic_add v1, v5, s[2:3]
	s_branch .Lgbw_1

; __device__ __forceinline__ unsigned xb_ld(unsigned* p)              { return __hip_atomic_load(p, __ATOMIC_RELAXED, __HIP_MEMORY_SCOPE_AGENT); }
; __device__ __forceinline__ unsigned xb_add(unsigned* p, unsigned v) { return __hip_atomic_fetch_add(p, v, __ATOMIC_RELAXED, __HIP_MEMORY_SCOPE_AGENT); }
; #define XB_SPIN(cond, bar) do { unsigned _sp = 0; while (cond) { __builtin_amdgcn_s_sleep(1); \
;     if ((++_sp & 255u) == 0u) { if (xb_ld(&(bar)[XB_TMO])) break; if (_sp > XB_SPIN_CAP) { atomicAdd(&(bar)[XB_TMO], 1u); break; } } } } while (0)
; __device__ __forceinline__ void xcd_barrier(const XcdBarrier& b) {
;     asm volatile("s_waitcnt vmcnt(0)" ::: "memory");
;     __syncthreads();
;     if (threadIdx.x == 0) {
;         unsigned* bar = b.bar;
;         __builtin_amdgcn_s_waitcnt(0);
;         unsigned nloc = b.st[0], nx = b.st[1];
;         if (nloc == 0u) { xcd_barrier_complete(bar, b.x, nloc, nx); b.st[0] = nloc; b.st[1] = nx; }
;         const unsigned old = xb_add(&bar[XB_XSUB(b.x)], 1u);
;         const unsigned gen = old / nloc;
;         if (old + 1u == (gen + 1u) * nloc) {
;             __builtin_amdgcn_fence(__ATOMIC_RELEASE, "agent");
;             asm volatile("s_waitcnt vmcnt(0)" ::: "memory");
;             const unsigned og = xb_add(&bar[XB_TOP], 1u);
;             const unsigned tg = og / nx;
;             if (og + 1u == (tg + 1u) * nx) xb_add(&bar[XB_TOPGEN], 1u);
;             else XB_SPIN(xb_ld(&bar[XB_TOPGEN]) == tg, bar);
;             __builtin_amdgcn_fence(__ATOMIC_ACQUIRE, "agent");
;             xb_add(&bar[XB_XGEN(b.x)], 1u);
;             asm volatile("s_waitcnt vmcnt(0)" ::: "memory");
;         } else {
;             XB_SPIN(xb_ld(&bar[XB_XGEN(b.x)]) == gen, bar);
;             __builtin_amdgcn_fence(__ATOMIC_ACQUIRE, "agent");
;             asm volatile("s_waitcnt vmcnt(0)" ::: "memory");
;         }
.LBB0_395:
	s_waitcnt lgkmcnt(0)
	v_readfirstlane_b32 s8, v3
	v_readfirstlane_b32 s9, v1
	v_readlane_b32 s0, v252, 4
	s_lshl_b32 s0, s0, 8
	v_readlane_b32 s2, v252, 2
	v_readlane_b32 s3, v252, 3
	s_add_u32 s6, s2, s0
	s_addc_u32 s7, s3, 0
	s_mul_i32 s10, s8, 3
	s_mul_i32 s11, s9, 3
	v_mov_b32_e32 v4, 0x1000
	v_mov_b32_e32 v5, 1
	global_atomic_add v4, v4, v5, s[6:7] offset:1024 sc0
	v_mov_b32_e32 v1, 0x3400
	s_waitcnt vmcnt(0)
	v_readfirstlane_b32 s0, v4
	s_add_u32 s0, s0, 1
	s_cmp_lg_u32 s0, s10
	s_cbranch_scc1 .Lgbn_2
	buffer_wbl2 sc1
	buffer_inv sc1
	s_waitcnt vmcnt(0)
	global_atomic_add v1, v5, s[2:3]
	s_branch .Lgbw_2

; __device__ __forceinline__ unsigned xb_ld(unsigned* p)              { return __hip_atomic_load(p, __ATOMIC_RELAXED, __HIP_MEMORY_SCOPE_AGENT); }
; __device__ __forceinline__ unsigned xb_add(unsigned* p, unsigned v) { return __hip_atomic_fetch_add(p, v, __ATOMIC_RELAXED, __HIP_MEMORY_SCOPE_AGENT); }
; #define XB_SPIN(cond, bar) do { unsigned _sp = 0; while (cond) { __builtin_amdgcn_s_sleep(1); \
;     if ((++_sp & 255u) == 0u) { if (xb_ld(&(bar)[XB_TMO])) break; if (_sp > XB_SPIN_CAP) { atomicAdd(&(bar)[XB_TMO], 1u); break; } } } } while (0)
; __device__ __forceinline__ void xcd_barrier(const XcdBarrier& b) {
;     asm volatile("s_waitcnt vmcnt(0)" ::: "memory");
;     __syncthreads();
;     if (threadIdx.x == 0) {
;         unsigned* bar = b.bar;
;         __builtin_amdgcn_s_waitcnt(0);
;         unsigned nloc = b.st[0], nx = b.st[1];
;         if (nloc == 0u) { xcd_barrier_complete(bar, b.x, nloc, nx); b.st[0] = nloc; b.st[1] = nx; }
;         const unsigned old = xb_add(&bar[XB_XSUB(b.x)], 1u);
;         const unsigned gen = old / nloc;
;         if (old + 1u == (gen + 1u) * nloc) {
;             __builtin_amdgcn_fence(__ATOMIC_RELEASE, "agent");
;             asm volatile("s_waitcnt vmcnt(0)" ::: "memory");
;             const unsigned og = xb_add(&bar[XB_TOP], 1u);
;             const unsigned tg = og / nx;
;             if (og + 1u == (tg + 1u) * nx) xb_add(&bar[XB_TOPGEN], 1u);
;             else XB_SPIN(xb_ld(&bar[XB_TOPGEN]) == tg, bar);
;             __builtin_amdgcn_fence(__ATOMIC_ACQUIRE, "agent");
;             xb_add(&bar[XB_XGEN(b.x)], 1u);
;             asm volatile("s_waitcnt vmcnt(0)" ::: "memory");
;         } else {
;             XB_SPIN(xb_ld(&bar[XB_XGEN(b.x)]) == gen, bar);
;             __builtin_amdgcn_fence(__ATOMIC_ACQUIRE, "agent");
;             asm volatile("s_waitcnt vmcnt(0)" ::: "memory");
;         }
.LBB0_489:
	s_waitcnt lgkmcnt(0)
	v_readfirstlane_b32 s8, v3
	v_readfirstlane_b32 s9, v1
	v_readlane_b32 s0, v252, 4
	s_lshl_b32 s0, s0, 8
	v_readlane_b32 s2, v252, 2
	v_readlane_b32 s3, v252, 3
	s_add_u32 s6, s2, s0
	s_addc_u32 s7, s3, 0
	s_mul_i32 s10, s8, 4
	s_mul_i32 s11, s9, 4
	v_mov_b32_e32 v4, 0x1000
	v_mov_b32_e32 v5, 1
	global_atomic_add v4, v4, v5, s[6:7] offset:1024 sc0
	v_mov_b32_e32 v1, 0x3400
	s_waitcnt vmcnt(0)
	v_readfirstlane_b32 s0, v4
	s_add_u32 s0, s0, 1
	s_cmp_lg_u32 s0, s10
	s_cbranch_scc1 .Lgbn_3
	buffer_wbl2 sc1
	buffer_inv sc1
	s_waitcnt vmcnt(0)
	global_atomic_add v1, v5, s[2:3]
	s_branch .Lgbw_3

; __device__ __forceinline__ unsigned xb_ld(unsigned* p)              { return __hip_atomic_load(p, __ATOMIC_RELAXED, __HIP_MEMORY_SCOPE_AGENT); }
; __device__ __forceinline__ unsigned xb_add(unsigned* p, unsigned v) { return __hip_atomic_fetch_add(p, v, __ATOMIC_RELAXED, __HIP_MEMORY_SCOPE_AGENT); }
; #define XB_SPIN(cond, bar) do { unsigned _sp = 0; while (cond) { __builtin_amdgcn_s_sleep(1); \
;     if ((++_sp & 255u) == 0u) { if (xb_ld(&(bar)[XB_TMO])) break; if (_sp > XB_SPIN_CAP) { atomicAdd(&(bar)[XB_TMO], 1u); break; } } } } while (0)
; __device__ __forceinline__ void xcd_barrier(const XcdBarrier& b) {
;     asm volatile("s_waitcnt vmcnt(0)" ::: "memory");
;     __syncthreads();
;     if (threadIdx.x == 0) {
;         unsigned* bar = b.bar;
;         __builtin_amdgcn_s_waitcnt(0);
;         unsigned nloc = b.st[0], nx = b.st[1];
;         if (nloc == 0u) { xcd_barrier_complete(bar, b.x, nloc, nx); b.st[0] = nloc; b.st[1] = nx; }
;         const unsigned old = xb_add(&bar[XB_XSUB(b.x)], 1u);
;         const unsigned gen = old / nloc;
;         if (old + 1u == (gen + 1u) * nloc) {
;             __builtin_amdgcn_fence(__ATOMIC_RELEASE, "agent");
;             asm volatile("s_waitcnt vmcnt(0)" ::: "memory");
;             const unsigned og = xb_add(&bar[XB_TOP], 1u);
;             const unsigned tg = og / nx;
;             if (og + 1u == (tg + 1u) * nx) xb_add(&bar[XB_TOPGEN], 1u);
;             else XB_SPIN(xb_ld(&bar[XB_TOPGEN]) == tg, bar);
;             __builtin_amdgcn_fence(__ATOMIC_ACQUIRE, "agent");
;             xb_add(&bar[XB_XGEN(b.x)], 1u);
;             asm volatile("s_waitcnt vmcnt(0)" ::: "memory");
;         } else {
;             XB_SPIN(xb_ld(&bar[XB_XGEN(b.x)]) == gen, bar);
;             __builtin_amdgcn_fence(__ATOMIC_ACQUIRE, "agent");
;             asm volatile("s_waitcnt vmcnt(0)" ::: "memory");
;         }
.LBB0_605:
	s_waitcnt lgkmcnt(0)
	v_readfirstlane_b32 s8, v3
	v_readfirstlane_b32 s9, v1
	v_readlane_b32 s0, v252, 4
	s_lshl_b32 s0, s0, 8
	v_readlane_b32 s2, v252, 2
	v_readlane_b32 s3, v252, 3
	s_add_u32 s6, s2, s0
	s_addc_u32 s7, s3, 0
	s_mul_i32 s10, s8, 5
	s_mul_i32 s11, s9, 5
	v_mov_b32_e32 v4, 0x1000
	v_mov_b32_e32 v5, 1
	global_atomic_add v4, v4, v5, s[6:7] offset:1024 sc0
	v_mov_b32_e32 v1, 0x3400
	s_waitcnt vmcnt(0)
	v_readfirstlane_b32 s0, v4
	s_add_u32 s0, s0, 1
	s_cmp_lg_u32 s0, s10
	s_cbranch_scc1 .Lgbn_4
	buffer_wbl2 sc1
	buffer_inv sc1
	s_waitcnt vmcnt(0)
	global_atomic_add v1, v5, s[2:3]
	s_branch .Lgbw_4

; __device__ __forceinline__ unsigned xb_ld(unsigned* p)              { return __hip_atomic_load(p, __ATOMIC_RELAXED, __HIP_MEMORY_SCOPE_AGENT); }
; __device__ __forceinline__ unsigned xb_add(unsigned* p, unsigned v) { return __hip_atomic_fetch_add(p, v, __ATOMIC_RELAXED, __HIP_MEMORY_SCOPE_AGENT); }
; #define XB_SPIN(cond, bar) do { unsigned _sp = 0; while (cond) { __builtin_amdgcn_s_sleep(1); \
;     if ((++_sp & 255u) == 0u) { if (xb_ld(&(bar)[XB_TMO])) break; if (_sp > XB_SPIN_CAP) { atomicAdd(&(bar)[XB_TMO], 1u); break; } } } } while (0)
; __device__ __forceinline__ void xcd_barrier(const XcdBarrier& b) {
;     asm volatile("s_waitcnt vmcnt(0)" ::: "memory");
;     __syncthreads();
;     if (threadIdx.x == 0) {
;         unsigned* bar = b.bar;
;         __builtin_amdgcn_s_waitcnt(0);
;         unsigned nloc = b.st[0], nx = b.st[1];
;         if (nloc == 0u) { xcd_barrier_complete(bar, b.x, nloc, nx); b.st[0] = nloc; b.st[1] = nx; }
;         const unsigned old = xb_add(&bar[XB_XSUB(b.x)], 1u);
;         const unsigned gen = old / nloc;
;         if (old + 1u == (gen + 1u) * nloc) {
;             __builtin_amdgcn_fence(__ATOMIC_RELEASE, "agent");
;             asm volatile("s_waitcnt vmcnt(0)" ::: "memory");
;             const unsigned og = xb_add(&bar[XB_TOP], 1u);
;             const unsigned tg = og / nx;
;             if (og + 1u == (tg + 1u) * nx) xb_add(&bar[XB_TOPGEN], 1u);
;             else XB_SPIN(xb_ld(&bar[XB_TOPGEN]) == tg, bar);
;             __builtin_amdgcn_fence(__ATOMIC_ACQUIRE, "agent");
;             xb_add(&bar[XB_XGEN(b.x)], 1u);
;             asm volatile("s_waitcnt vmcnt(0)" ::: "memory");
;         } else {
;             XB_SPIN(xb_ld(&bar[XB_XGEN(b.x)]) == gen, bar);
;             __builtin_amdgcn_fence(__ATOMIC_ACQUIRE, "agent");
;             asm volatile("s_waitcnt vmcnt(0)" ::: "memory");
;         }
.LBB0_691:
	s_waitcnt lgkmcnt(0)
	v_readfirstlane_b32 s8, v3
	v_readfirstlane_b32 s9, v1
	v_readlane_b32 s0, v252, 4
	s_lshl_b32 s0, s0, 8
	v_readlane_b32 s2, v252, 2
	v_readlane_b32 s3, v252, 3
	s_add_u32 s6, s2, s0
	s_addc_u32 s7, s3, 0
	s_mul_i32 s10, s8, 6
	s_mul_i32 s11, s9, 6
	v_mov_b32_e32 v4, 0x1000
	v_mov_b32_e32 v5, 1
	global_atomic_add v4, v4, v5, s[6:7] offset:1024 sc0
	v_mov_b32_e32 v1, 0x3400
	s_waitcnt vmcnt(0)
	v_readfirstlane_b32 s0, v4
	s_add_u32 s0, s0, 1
	s_cmp_lg_u32 s0, s10
	s_cbranch_scc1 .Lgbn_5
	buffer_wbl2 sc1
	buffer_inv sc1
	s_waitcnt vmcnt(0)
	global_atomic_add v1, v5, s[2:3]
	s_branch .Lgbw_5

; __device__ __forceinline__ unsigned xb_ld(unsigned* p)              { return __hip_atomic_load(p, __ATOMIC_RELAXED, __HIP_MEMORY_SCOPE_AGENT); }
; __device__ __forceinline__ unsigned xb_add(unsigned* p, unsigned v) { return __hip_atomic_fetch_add(p, v, __ATOMIC_RELAXED, __HIP_MEMORY_SCOPE_AGENT); }
; #define XB_SPIN(cond, bar) do { unsigned _sp = 0; while (cond) { __builtin_amdgcn_s_sleep(1); \
;     if ((++_sp & 255u) == 0u) { if (xb_ld(&(bar)[XB_TMO])) break; if (_sp > XB_SPIN_CAP) { atomicAdd(&(bar)[XB_TMO], 1u); break; } } } } while (0)
; __device__ __forceinline__ void xcd_barrier(const XcdBarrier& b) {
;     asm volatile("s_waitcnt vmcnt(0)" ::: "memory");
;     __syncthreads();
;     if (threadIdx.x == 0) {
;         unsigned* bar = b.bar;
;         __builtin_amdgcn_s_waitcnt(0);
;         unsigned nloc = b.st[0], nx = b.st[1];
;         if (nloc == 0u) { xcd_barrier_complete(bar, b.x, nloc, nx); b.st[0] = nloc; b.st[1] = nx; }
;         const unsigned old = xb_add(&bar[XB_XSUB(b.x)], 1u);
;         const unsigned gen = old / nloc;
;         if (old + 1u == (gen + 1u) * nloc) {
;             __builtin_amdgcn_fence(__ATOMIC_RELEASE, "agent");
;             asm volatile("s_waitcnt vmcnt(0)" ::: "memory");
;             const unsigned og = xb_add(&bar[XB_TOP], 1u);
;             const unsigned tg = og / nx;
;             if (og + 1u == (tg + 1u) * nx) xb_add(&bar[XB_TOPGEN], 1u);
;             else XB_SPIN(xb_ld(&bar[XB_TOPGEN]) == tg, bar);
;             __builtin_amdgcn_fence(__ATOMIC_ACQUIRE, "agent");
;             xb_add(&bar[XB_XGEN(b.x)], 1u);
;             asm volatile("s_waitcnt vmcnt(0)" ::: "memory");
;         } else {
;             XB_SPIN(xb_ld(&bar[XB_XGEN(b.x)]) == gen, bar);
;             __builtin_amdgcn_fence(__ATOMIC_ACQUIRE, "agent");
;             asm volatile("s_waitcnt vmcnt(0)" ::: "memory");
;         }
.LBB0_759:
	s_waitcnt lgkmcnt(0)
	v_readfirstlane_b32 s8, v3
	v_readfirstlane_b32 s9, v1
	v_readlane_b32 s0, v252, 4
	s_lshl_b32 s0, s0, 8
	v_readlane_b32 s2, v252, 2
	v_readlane_b32 s3, v252, 3
	s_add_u32 s6, s2, s0
	s_addc_u32 s7, s3, 0
	s_mul_i32 s10, s8, 7
	s_mul_i32 s11, s9, 7
	v_mov_b32_e32 v4, 0x1000
	v_mov_b32_e32 v5, 1
	global_atomic_add v4, v4, v5, s[6:7] offset:1024 sc0
	v_mov_b32_e32 v1, 0x3400
	s_waitcnt vmcnt(0)
	v_readfirstlane_b32 s0, v4
	s_add_u32 s0, s0, 1
	s_cmp_lg_u32 s0, s10
	s_cbranch_scc1 .Lgbn_6
	buffer_wbl2 sc1
	buffer_inv sc1
	s_waitcnt vmcnt(0)
	global_atomic_add v1, v5, s[2:3]
	s_branch .Lgbw_6

; __device__ __forceinline__ unsigned xb_ld(unsigned* p)              { return __hip_atomic_load(p, __ATOMIC_RELAXED, __HIP_MEMORY_SCOPE_AGENT); }
; __device__ __forceinline__ unsigned xb_add(unsigned* p, unsigned v) { return __hip_atomic_fetch_add(p, v, __ATOMIC_RELAXED, __HIP_MEMORY_SCOPE_AGENT); }
; #define XB_SPIN(cond, bar) do { unsigned _sp = 0; while (cond) { __builtin_amdgcn_s_sleep(1); \
;     if ((++_sp & 255u) == 0u) { if (xb_ld(&(bar)[XB_TMO])) break; if (_sp > XB_SPIN_CAP) { atomicAdd(&(bar)[XB_TMO], 1u); break; } } } } while (0)
; __device__ __forceinline__ void xcd_barrier(const XcdBarrier& b) {
;     asm volatile("s_waitcnt vmcnt(0)" ::: "memory");
;     __syncthreads();
;     if (threadIdx.x == 0) {
;         unsigned* bar = b.bar;
;         __builtin_amdgcn_s_waitcnt(0);
;         unsigned nloc = b.st[0], nx = b.st[1];
;         if (nloc == 0u) { xcd_barrier_complete(bar, b.x, nloc, nx); b.st[0] = nloc; b.st[1] = nx; }
;         const unsigned old = xb_add(&bar[XB_XSUB(b.x)], 1u);
;         const unsigned gen = old / nloc;
;         if (old + 1u == (gen + 1u) * nloc) {
;             __builtin_amdgcn_fence(__ATOMIC_RELEASE, "agent");
;             asm volatile("s_waitcnt vmcnt(0)" ::: "memory");
;             const unsigned og = xb_add(&bar[XB_TOP], 1u);
;             const unsigned tg = og / nx;
;             if (og + 1u == (tg + 1u) * nx) xb_add(&bar[XB_TOPGEN], 1u);
;             else XB_SPIN(xb_ld(&bar[XB_TOPGEN]) == tg, bar);
;             __builtin_amdgcn_fence(__ATOMIC_ACQUIRE, "agent");
;             xb_add(&bar[XB_XGEN(b.x)], 1u);
;             asm volatile("s_waitcnt vmcnt(0)" ::: "memory");
;         } else {
;             XB_SPIN(xb_ld(&bar[XB_XGEN(b.x)]) == gen, bar);
;             __builtin_amdgcn_fence(__ATOMIC_ACQUIRE, "agent");
;             asm volatile("s_waitcnt vmcnt(0)" ::: "memory");
;         }
.LBB0_827:
	s_waitcnt lgkmcnt(0)
	v_readfirstlane_b32 s8, v3
	v_readfirstlane_b32 s9, v1
	v_readlane_b32 s0, v252, 4
	s_lshl_b32 s0, s0, 8
	v_readlane_b32 s2, v252, 2
	v_readlane_b32 s3, v252, 3
	s_add_u32 s6, s2, s0
	s_addc_u32 s7, s3, 0
	s_mul_i32 s10, s8, 8
	s_mul_i32 s11, s9, 8
	v_mov_b32_e32 v4, 0x1000
	v_mov_b32_e32 v5, 1
	global_atomic_add v4, v4, v5, s[6:7] offset:1024 sc0
	v_mov_b32_e32 v1, 0x3400
	s_waitcnt vmcnt(0)
	v_readfirstlane_b32 s0, v4
	s_add_u32 s0, s0, 1
	s_cmp_lg_u32 s0, s10
	s_cbranch_scc1 .Lgbn_7
	buffer_wbl2 sc1
	buffer_inv sc1
	s_waitcnt vmcnt(0)
	global_atomic_add v1, v5, s[2:3]
	s_branch .Lgbw_7

; __device__ __forceinline__ unsigned xb_ld(unsigned* p)              { return __hip_atomic_load(p, __ATOMIC_RELAXED, __HIP_MEMORY_SCOPE_AGENT); }
; __device__ __forceinline__ unsigned xb_add(unsigned* p, unsigned v) { return __hip_atomic_fetch_add(p, v, __ATOMIC_RELAXED, __HIP_MEMORY_SCOPE_AGENT); }
; #define XB_SPIN(cond, bar) do { unsigned _sp = 0; while (cond) { __builtin_amdgcn_s_sleep(1); \
;     if ((++_sp & 255u) == 0u) { if (xb_ld(&(bar)[XB_TMO])) break; if (_sp > XB_SPIN_CAP) { atomicAdd(&(bar)[XB_TMO], 1u); break; } } } } while (0)
; __device__ __forceinline__ void xcd_barrier(const XcdBarrier& b) {
;     asm volatile("s_waitcnt vmcnt(0)" ::: "memory");
;     __syncthreads();
;     if (threadIdx.x == 0) {
;         unsigned* bar = b.bar;
;         __builtin_amdgcn_s_waitcnt(0);
;         unsigned nloc = b.st[0], nx = b.st[1];
;         if (nloc == 0u) { xcd_barrier_complete(bar, b.x, nloc, nx); b.st[0] = nloc; b.st[1] = nx; }
;         const unsigned old = xb_add(&bar[XB_XSUB(b.x)], 1u);
;         const unsigned gen = old / nloc;
;         if (old + 1u == (gen + 1u) * nloc) {
;             __builtin_amdgcn_fence(__ATOMIC_RELEASE, "agent");
;             asm volatile("s_waitcnt vmcnt(0)" ::: "memory");
;             const unsigned og = xb_add(&bar[XB_TOP], 1u);
;             const unsigned tg = og / nx;
;             if (og + 1u == (tg + 1u) * nx) xb_add(&bar[XB_TOPGEN], 1u);
;             else XB_SPIN(xb_ld(&bar[XB_TOPGEN]) == tg, bar);
;             __builtin_amdgcn_fence(__ATOMIC_ACQUIRE, "agent");
;             xb_add(&bar[XB_XGEN(b.x)], 1u);
;             asm volatile("s_waitcnt vmcnt(0)" ::: "memory");
;         } else {
;             XB_SPIN(xb_ld(&bar[XB_XGEN(b.x)]) == gen, bar);
;             __builtin_amdgcn_fence(__ATOMIC_ACQUIRE, "agent");
;             asm volatile("s_waitcnt vmcnt(0)" ::: "memory");
;         }
.LBB0_961:
	s_waitcnt lgkmcnt(0)
	v_readfirstlane_b32 s8, v3
	v_readfirstlane_b32 s9, v1
	v_readlane_b32 s0, v252, 4
	s_lshl_b32 s0, s0, 8
	v_readlane_b32 s2, v252, 2
	v_readlane_b32 s3, v252, 3
	s_add_u32 s6, s2, s0
	s_addc_u32 s7, s3, 0
	s_mul_i32 s10, s8, 9
	s_mul_i32 s11, s9, 9
	v_mov_b32_e32 v4, 0x1000
	v_mov_b32_e32 v5, 1
	global_atomic_add v4, v4, v5, s[6:7] offset:1024 sc0
	v_mov_b32_e32 v1, 0x3400
	s_waitcnt vmcnt(0)
	v_readfirstlane_b32 s0, v4
	s_add_u32 s0, s0, 1
	s_cmp_lg_u32 s0, s10
	s_cbranch_scc1 .Lgbn_8
	buffer_wbl2 sc1
	buffer_inv sc1
	s_waitcnt vmcnt(0)
	global_atomic_add v1, v5, s[2:3]
	s_branch .Lgbw_8

; __device__ __forceinline__ unsigned xb_ld(unsigned* p)              { return __hip_atomic_load(p, __ATOMIC_RELAXED, __HIP_MEMORY_SCOPE_AGENT); }
; __device__ __forceinline__ unsigned xb_add(unsigned* p, unsigned v) { return __hip_atomic_fetch_add(p, v, __ATOMIC_RELAXED, __HIP_MEMORY_SCOPE_AGENT); }
; #define XB_SPIN(cond, bar) do { unsigned _sp = 0; while (cond) { __builtin_amdgcn_s_sleep(1); \
;     if ((++_sp & 255u) == 0u) { if (xb_ld(&(bar)[XB_TMO])) break; if (_sp > XB_SPIN_CAP) { atomicAdd(&(bar)[XB_TMO], 1u); break; } } } } while (0)
; __device__ __forceinline__ void xcd_barrier(const XcdBarrier& b) {
;     asm volatile("s_waitcnt vmcnt(0)" ::: "memory");
;     __syncthreads();
;     if (threadIdx.x == 0) {
;         unsigned* bar = b.bar;
;         __builtin_amdgcn_s_waitcnt(0);
;         unsigned nloc = b.st[0], nx = b.st[1];
;         if (nloc == 0u) { xcd_barrier_complete(bar, b.x, nloc, nx); b.st[0] = nloc; b.st[1] = nx; }
;         const unsigned old = xb_add(&bar[XB_XSUB(b.x)], 1u);
;         const unsigned gen = old / nloc;
;         if (old + 1u == (gen + 1u) * nloc) {
;             __builtin_amdgcn_fence(__ATOMIC_RELEASE, "agent");
;             asm volatile("s_waitcnt vmcnt(0)" ::: "memory");
;             const unsigned og = xb_add(&bar[XB_TOP], 1u);
;             const unsigned tg = og / nx;
;             if (og + 1u == (tg + 1u) * nx) xb_add(&bar[XB_TOPGEN], 1u);
;             else XB_SPIN(xb_ld(&bar[XB_TOPGEN]) == tg, bar);
;             __builtin_amdgcn_fence(__ATOMIC_ACQUIRE, "agent");
;             xb_add(&bar[XB_XGEN(b.x)], 1u);
;             asm volatile("s_waitcnt vmcnt(0)" ::: "memory");
;         } else {
;             XB_SPIN(xb_ld(&bar[XB_XGEN(b.x)]) == gen, bar);
;             __builtin_amdgcn_fence(__ATOMIC_ACQUIRE, "agent");
;             asm volatile("s_waitcnt vmcnt(0)" ::: "memory");
;         }
.LBB0_1105:
	s_waitcnt lgkmcnt(0)
	v_readfirstlane_b32 s8, v3
	v_readfirstlane_b32 s9, v1
	v_readlane_b32 s0, v252, 4
	s_lshl_b32 s0, s0, 8
	v_readlane_b32 s2, v252, 2
	v_readlane_b32 s3, v252, 3
	s_add_u32 s6, s2, s0
	s_addc_u32 s7, s3, 0
	s_mul_i32 s10, s8, 10
	s_mul_i32 s11, s9, 10
	v_mov_b32_e32 v4, 0x1000
	v_mov_b32_e32 v5, 1
	global_atomic_add v4, v4, v5, s[6:7] offset:1024 sc0
	v_mov_b32_e32 v1, 0x3400
	s_waitcnt vmcnt(0)
	v_readfirstlane_b32 s0, v4
	s_add_u32 s0, s0, 1
	s_cmp_lg_u32 s0, s10
	s_cbranch_scc1 .Lgbn_9
	buffer_wbl2 sc1
	buffer_inv sc1
	s_waitcnt vmcnt(0)
	global_atomic_add v1, v5, s[2:3]
	s_branch .Lgbw_9

; __device__ __forceinline__ unsigned xb_ld(unsigned* p)              { return __hip_atomic_load(p, __ATOMIC_RELAXED, __HIP_MEMORY_SCOPE_AGENT); }
; __device__ __forceinline__ unsigned xb_add(unsigned* p, unsigned v) { return __hip_atomic_fetch_add(p, v, __ATOMIC_RELAXED, __HIP_MEMORY_SCOPE_AGENT); }
; #define XB_SPIN(cond, bar) do { unsigned _sp = 0; while (cond) { __builtin_amdgcn_s_sleep(1); \
;     if ((++_sp & 255u) == 0u) { if (xb_ld(&(bar)[XB_TMO])) break; if (_sp > XB_SPIN_CAP) { atomicAdd(&(bar)[XB_TMO], 1u); break; } } } } while (0)
; __device__ __forceinline__ void xcd_barrier(const XcdBarrier& b) {
;     asm volatile("s_waitcnt vmcnt(0)" ::: "memory");
;     __syncthreads();
;     if (threadIdx.x == 0) {
;         unsigned* bar = b.bar;
;         __builtin_amdgcn_s_waitcnt(0);
;         unsigned nloc = b.st[0], nx = b.st[1];
;         if (nloc == 0u) { xcd_barrier_complete(bar, b.x, nloc, nx); b.st[0] = nloc; b.st[1] = nx; }
;         const unsigned old = xb_add(&bar[XB_XSUB(b.x)], 1u);
;         const unsigned gen = old / nloc;
;         if (old + 1u == (gen + 1u) * nloc) {
;             __builtin_amdgcn_fence(__ATOMIC_RELEASE, "agent");
;             asm volatile("s_waitcnt vmcnt(0)" ::: "memory");
;             const unsigned og = xb_add(&bar[XB_TOP], 1u);
;             const unsigned tg = og / nx;
;             if (og + 1u == (tg + 1u) * nx) xb_add(&bar[XB_TOPGEN], 1u);
;             else XB_SPIN(xb_ld(&bar[XB_TOPGEN]) == tg, bar);
;             __builtin_amdgcn_fence(__ATOMIC_ACQUIRE, "agent");
;             xb_add(&bar[XB_XGEN(b.x)], 1u);
;             asm volatile("s_waitcnt vmcnt(0)" ::: "memory");
;         } else {
;             XB_SPIN(xb_ld(&bar[XB_XGEN(b.x)]) == gen, bar);
;             __builtin_amdgcn_fence(__ATOMIC_ACQUIRE, "agent");
;             asm volatile("s_waitcnt vmcnt(0)" ::: "memory");
;         }
.LBB0_1192:
	s_waitcnt lgkmcnt(0)
	v_readfirstlane_b32 s8, v3
	v_readfirstlane_b32 s9, v1
	v_readlane_b32 s0, v252, 4
	s_lshl_b32 s0, s0, 8
	v_readlane_b32 s2, v252, 2
	v_readlane_b32 s3, v252, 3
	s_add_u32 s6, s2, s0
	s_addc_u32 s7, s3, 0
	s_mul_i32 s10, s8, 11
	s_mul_i32 s11, s9, 11
	v_mov_b32_e32 v4, 0x1000
	v_mov_b32_e32 v5, 1
	global_atomic_add v4, v4, v5, s[6:7] offset:1024 sc0
	v_mov_b32_e32 v1, 0x3400
	s_waitcnt vmcnt(0)
	v_readfirstlane_b32 s0, v4
	s_add_u32 s0, s0, 1
	s_cmp_lg_u32 s0, s10
	s_cbranch_scc1 .Lgbn_10
	buffer_wbl2 sc1
	buffer_inv sc1
	s_waitcnt vmcnt(0)
	global_atomic_add v1, v5, s[2:3]
	s_branch .Lgbw_10

; __device__ __forceinline__ unsigned xb_ld(unsigned* p)              { return __hip_atomic_load(p, __ATOMIC_RELAXED, __HIP_MEMORY_SCOPE_AGENT); }
; __device__ __forceinline__ unsigned xb_add(unsigned* p, unsigned v) { return __hip_atomic_fetch_add(p, v, __ATOMIC_RELAXED, __HIP_MEMORY_SCOPE_AGENT); }
; #define XB_SPIN(cond, bar) do { unsigned _sp = 0; while (cond) { __builtin_amdgcn_s_sleep(1); \
;     if ((++_sp & 255u) == 0u) { if (xb_ld(&(bar)[XB_TMO])) break; if (_sp > XB_SPIN_CAP) { atomicAdd(&(bar)[XB_TMO], 1u); break; } } } } while (0)
; __device__ __forceinline__ void xcd_barrier(const XcdBarrier& b) {
;     asm volatile("s_waitcnt vmcnt(0)" ::: "memory");
;     __syncthreads();
;     if (threadIdx.x == 0) {
;         unsigned* bar = b.bar;
;         __builtin_amdgcn_s_waitcnt(0);
;         unsigned nloc = b.st[0], nx = b.st[1];
;         if (nloc == 0u) { xcd_barrier_complete(bar, b.x, nloc, nx); b.st[0] = nloc; b.st[1] = nx; }
;         const unsigned old = xb_add(&bar[XB_XSUB(b.x)], 1u);
;         const unsigned gen = old / nloc;
;         if (old + 1u == (gen + 1u) * nloc) {
;             __builtin_amdgcn_fence(__ATOMIC_RELEASE, "agent");
;             asm volatile("s_waitcnt vmcnt(0)" ::: "memory");
;             const unsigned og = xb_add(&bar[XB_TOP], 1u);
;             const unsigned tg = og / nx;
;             if (og + 1u == (tg + 1u) * nx) xb_add(&bar[XB_TOPGEN], 1u);
;             else XB_SPIN(xb_ld(&bar[XB_TOPGEN]) == tg, bar);
;             __builtin_amdgcn_fence(__ATOMIC_ACQUIRE, "agent");
;             xb_add(&bar[XB_XGEN(b.x)], 1u);
;             asm volatile("s_waitcnt vmcnt(0)" ::: "memory");
;         } else {
;             XB_SPIN(xb_ld(&bar[XB_XGEN(b.x)]) == gen, bar);
;             __builtin_amdgcn_fence(__ATOMIC_ACQUIRE, "agent");
;             asm volatile("s_waitcnt vmcnt(0)" ::: "memory");
;         }
.LBB0_1314:
	s_waitcnt lgkmcnt(0)
	v_readfirstlane_b32 s8, v3
	v_readfirstlane_b32 s9, v1
	v_readlane_b32 s0, v252, 4
	s_lshl_b32 s0, s0, 8
	v_readlane_b32 s2, v252, 2
	v_readlane_b32 s3, v252, 3
	s_add_u32 s6, s2, s0
	s_addc_u32 s7, s3, 0
	s_mul_i32 s10, s8, 12
	s_mul_i32 s11, s9, 12
	v_mov_b32_e32 v4, 0x1000
	v_mov_b32_e32 v5, 1
	global_atomic_add v4, v4, v5, s[6:7] offset:1024 sc0
	v_mov_b32_e32 v1, 0x3400
	s_waitcnt vmcnt(0)
	v_readfirstlane_b32 s0, v4
	s_add_u32 s0, s0, 1
	s_cmp_lg_u32 s0, s10
	s_cbranch_scc1 .Lgbn_11
	buffer_wbl2 sc1
	buffer_inv sc1
	s_waitcnt vmcnt(0)
	global_atomic_add v1, v5, s[2:3]
	s_branch .Lgbw_11

; __device__ __forceinline__ unsigned xb_ld(unsigned* p)              { return __hip_atomic_load(p, __ATOMIC_RELAXED, __HIP_MEMORY_SCOPE_AGENT); }
; __device__ __forceinline__ unsigned xb_add(unsigned* p, unsigned v) { return __hip_atomic_fetch_add(p, v, __ATOMIC_RELAXED, __HIP_MEMORY_SCOPE_AGENT); }
; #define XB_SPIN(cond, bar) do { unsigned _sp = 0; while (cond) { __builtin_amdgcn_s_sleep(1); \
;     if ((++_sp & 255u) == 0u) { if (xb_ld(&(bar)[XB_TMO])) break; if (_sp > XB_SPIN_CAP) { atomicAdd(&(bar)[XB_TMO], 1u); break; } } } } while (0)
; __device__ __forceinline__ void xcd_barrier(const XcdBarrier& b) {
;     asm volatile("s_waitcnt vmcnt(0)" ::: "memory");
;     __syncthreads();
;     if (threadIdx.x == 0) {
;         unsigned* bar = b.bar;
;         __builtin_amdgcn_s_waitcnt(0);
;         unsigned nloc = b.st[0], nx = b.st[1];
;         if (nloc == 0u) { xcd_barrier_complete(bar, b.x, nloc, nx); b.st[0] = nloc; b.st[1] = nx; }
;         const unsigned old = xb_add(&bar[XB_XSUB(b.x)], 1u);
;         const unsigned gen = old / nloc;
;         if (old + 1u == (gen + 1u) * nloc) {
;             __builtin_amdgcn_fence(__ATOMIC_RELEASE, "agent");
;             asm volatile("s_waitcnt vmcnt(0)" ::: "memory");
;             const unsigned og = xb_add(&bar[XB_TOP], 1u);
;             const unsigned tg = og / nx;
;             if (og + 1u == (tg + 1u) * nx) xb_add(&bar[XB_TOPGEN], 1u);
;             else XB_SPIN(xb_ld(&bar[XB_TOPGEN]) == tg, bar);
;             __builtin_amdgcn_fence(__ATOMIC_ACQUIRE, "agent");
;             xb_add(&bar[XB_XGEN(b.x)], 1u);
;             asm volatile("s_waitcnt vmcnt(0)" ::: "memory");
;         } else {
;             XB_SPIN(xb_ld(&bar[XB_XGEN(b.x)]) == gen, bar);
;             __builtin_amdgcn_fence(__ATOMIC_ACQUIRE, "agent");
;             asm volatile("s_waitcnt vmcnt(0)" ::: "memory");
;         }
.LBB0_1381:
	s_waitcnt lgkmcnt(0)
	v_readfirstlane_b32 s8, v3
	v_readfirstlane_b32 s9, v1
	v_readlane_b32 s0, v252, 4
	s_lshl_b32 s0, s0, 8
	v_readlane_b32 s2, v252, 2
	v_readlane_b32 s3, v252, 3
	s_add_u32 s6, s2, s0
	s_addc_u32 s7, s3, 0
	s_mul_i32 s10, s8, 13
	s_mul_i32 s11, s9, 13
	v_mov_b32_e32 v4, 0x1000
	v_mov_b32_e32 v5, 1
	global_atomic_add v4, v4, v5, s[6:7] offset:1024 sc0
	v_mov_b32_e32 v1, 0x3400
	s_waitcnt vmcnt(0)
	v_readfirstlane_b32 s0, v4
	s_add_u32 s0, s0, 1
	s_cmp_lg_u32 s0, s10
	s_cbranch_scc1 .Lgbn_12
	buffer_wbl2 sc1
	buffer_inv sc1
	s_waitcnt vmcnt(0)
	global_atomic_add v1, v5, s[2:3]
	s_branch .Lgbw_12

; __device__ __forceinline__ unsigned xb_ld(unsigned* p)              { return __hip_atomic_load(p, __ATOMIC_RELAXED, __HIP_MEMORY_SCOPE_AGENT); }
; __device__ __forceinline__ unsigned xb_add(unsigned* p, unsigned v) { return __hip_atomic_fetch_add(p, v, __ATOMIC_RELAXED, __HIP_MEMORY_SCOPE_AGENT); }
; #define XB_SPIN(cond, bar) do { unsigned _sp = 0; while (cond) { __builtin_amdgcn_s_sleep(1); \
;     if ((++_sp & 255u) == 0u) { if (xb_ld(&(bar)[XB_TMO])) break; if (_sp > XB_SPIN_CAP) { atomicAdd(&(bar)[XB_TMO], 1u); break; } } } } while (0)
; __device__ __forceinline__ void xcd_barrier(const XcdBarrier& b) {
;     asm volatile("s_waitcnt vmcnt(0)" ::: "memory");
;     __syncthreads();
;     if (threadIdx.x == 0) {
;         unsigned* bar = b.bar;
;         __builtin_amdgcn_s_waitcnt(0);
;         unsigned nloc = b.st[0], nx = b.st[1];
;         if (nloc == 0u) { xcd_barrier_complete(bar, b.x, nloc, nx); b.st[0] = nloc; b.st[1] = nx; }
;         const unsigned old = xb_add(&bar[XB_XSUB(b.x)], 1u);
;         const unsigned gen = old / nloc;
;         if (old + 1u == (gen + 1u) * nloc) {
;             __builtin_amdgcn_fence(__ATOMIC_RELEASE, "agent");
;             asm volatile("s_waitcnt vmcnt(0)" ::: "memory");
;             const unsigned og = xb_add(&bar[XB_TOP], 1u);
;             const unsigned tg = og / nx;
;             if (og + 1u == (tg + 1u) * nx) xb_add(&bar[XB_TOPGEN], 1u);
;             else XB_SPIN(xb_ld(&bar[XB_TOPGEN]) == tg, bar);
;             __builtin_amdgcn_fence(__ATOMIC_ACQUIRE, "agent");
;             xb_add(&bar[XB_XGEN(b.x)], 1u);
;             asm volatile("s_waitcnt vmcnt(0)" ::: "memory");
;         } else {
;             XB_SPIN(xb_ld(&bar[XB_XGEN(b.x)]) == gen, bar);
;             __builtin_amdgcn_fence(__ATOMIC_ACQUIRE, "agent");
;             asm volatile("s_waitcnt vmcnt(0)" ::: "memory");
;         }
.LBB0_1499:
	s_waitcnt lgkmcnt(0)
	v_readfirstlane_b32 s8, v3
	v_readfirstlane_b32 s9, v1
	v_readlane_b32 s0, v252, 4
	s_lshl_b32 s0, s0, 8
	v_readlane_b32 s2, v252, 2
	v_readlane_b32 s3, v252, 3
	s_add_u32 s6, s2, s0
	s_addc_u32 s7, s3, 0
	s_mul_i32 s10, s8, 14
	s_mul_i32 s11, s9, 14
	v_mov_b32_e32 v4, 0x1000
	v_mov_b32_e32 v5, 1
	global_atomic_add v4, v4, v5, s[6:7] offset:1024 sc0
	v_mov_b32_e32 v1, 0x3400
	s_waitcnt vmcnt(0)
	v_readfirstlane_b32 s0, v4
	s_add_u32 s0, s0, 1
	s_cmp_lg_u32 s0, s10
	s_cbranch_scc1 .Lgbn_13
	buffer_wbl2 sc1
	buffer_inv sc1
	s_waitcnt vmcnt(0)
	global_atomic_add v1, v5, s[2:3]
	s_branch .Lgbw_13

; __device__ __forceinline__ unsigned xb_ld(unsigned* p)              { return __hip_atomic_load(p, __ATOMIC_RELAXED, __HIP_MEMORY_SCOPE_AGENT); }
; __device__ __forceinline__ unsigned xb_add(unsigned* p, unsigned v) { return __hip_atomic_fetch_add(p, v, __ATOMIC_RELAXED, __HIP_MEMORY_SCOPE_AGENT); }
; #define XB_SPIN(cond, bar) do { unsigned _sp = 0; while (cond) { __builtin_amdgcn_s_sleep(1); \
;     if ((++_sp & 255u) == 0u) { if (xb_ld(&(bar)[XB_TMO])) break; if (_sp > XB_SPIN_CAP) { atomicAdd(&(bar)[XB_TMO], 1u); break; } } } } while (0)
; __device__ __forceinline__ void xcd_barrier(const XcdBarrier& b) {
;     asm volatile("s_waitcnt vmcnt(0)" ::: "memory");
;     __syncthreads();
;     if (threadIdx.x == 0) {
;         unsigned* bar = b.bar;
;         __builtin_amdgcn_s_waitcnt(0);
;         unsigned nloc = b.st[0], nx = b.st[1];
;         if (nloc == 0u) { xcd_barrier_complete(bar, b.x, nloc, nx); b.st[0] = nloc; b.st[1] = nx; }
;         const unsigned old = xb_add(&bar[XB_XSUB(b.x)], 1u);
;         const unsigned gen = old / nloc;
;         if (old + 1u == (gen + 1u) * nloc) {
;             __builtin_amdgcn_fence(__ATOMIC_RELEASE, "agent");
;             asm volatile("s_waitcnt vmcnt(0)" ::: "memory");
;             const unsigned og = xb_add(&bar[XB_TOP], 1u);
;             const unsigned tg = og / nx;
;             if (og + 1u == (tg + 1u) * nx) xb_add(&bar[XB_TOPGEN], 1u);
;             else XB_SPIN(xb_ld(&bar[XB_TOPGEN]) == tg, bar);
;             __builtin_amdgcn_fence(__ATOMIC_ACQUIRE, "agent");
;             xb_add(&bar[XB_XGEN(b.x)], 1u);
;             asm volatile("s_waitcnt vmcnt(0)" ::: "memory");
;         } else {
;             XB_SPIN(xb_ld(&bar[XB_XGEN(b.x)]) == gen, bar);
;             __builtin_amdgcn_fence(__ATOMIC_ACQUIRE, "agent");
;             asm volatile("s_waitcnt vmcnt(0)" ::: "memory");
;         }
.LBB0_1585:
	s_waitcnt lgkmcnt(0)
	v_readfirstlane_b32 s8, v3
	v_readfirstlane_b32 s9, v1
	v_readlane_b32 s0, v252, 4
	s_lshl_b32 s0, s0, 8
	v_readlane_b32 s2, v252, 2
	v_readlane_b32 s3, v252, 3
	s_add_u32 s6, s2, s0
	s_addc_u32 s7, s3, 0
	s_mul_i32 s10, s8, 15
	s_mul_i32 s11, s9, 15
	v_mov_b32_e32 v4, 0x1000
	v_mov_b32_e32 v5, 1
	global_atomic_add v4, v4, v5, s[6:7] offset:1024 sc0
	v_mov_b32_e32 v1, 0x3400
	s_waitcnt vmcnt(0)
	v_readfirstlane_b32 s0, v4
	s_add_u32 s0, s0, 1
	s_cmp_lg_u32 s0, s10
	s_cbranch_scc1 .Lgbn_14
	buffer_wbl2 sc1
	buffer_inv sc1
	s_waitcnt vmcnt(0)
	global_atomic_add v1, v5, s[2:3]
	s_branch .Lgbw_14

; __device__ __forceinline__ unsigned xb_ld(unsigned* p)              { return __hip_atomic_load(p, __ATOMIC_RELAXED, __HIP_MEMORY_SCOPE_AGENT); }
; __device__ __forceinline__ unsigned xb_add(unsigned* p, unsigned v) { return __hip_atomic_fetch_add(p, v, __ATOMIC_RELAXED, __HIP_MEMORY_SCOPE_AGENT); }
; #define XB_SPIN(cond, bar) do { unsigned _sp = 0; while (cond) { __builtin_amdgcn_s_sleep(1); \
;     if ((++_sp & 255u) == 0u) { if (xb_ld(&(bar)[XB_TMO])) break; if (_sp > XB_SPIN_CAP) { atomicAdd(&(bar)[XB_TMO], 1u); break; } } } } while (0)
; __device__ __forceinline__ void xcd_barrier(const XcdBarrier& b) {
;     asm volatile("s_waitcnt vmcnt(0)" ::: "memory");
;     __syncthreads();
;     if (threadIdx.x == 0) {
;         unsigned* bar = b.bar;
;         __builtin_amdgcn_s_waitcnt(0);
;         unsigned nloc = b.st[0], nx = b.st[1];
;         if (nloc == 0u) { xcd_barrier_complete(bar, b.x, nloc, nx); b.st[0] = nloc; b.st[1] = nx; }
;         const unsigned old = xb_add(&bar[XB_XSUB(b.x)], 1u);
;         const unsigned gen = old / nloc;
;         if (old + 1u == (gen + 1u) * nloc) {
;             __builtin_amdgcn_fence(__ATOMIC_RELEASE, "agent");
;             asm volatile("s_waitcnt vmcnt(0)" ::: "memory");
;             const unsigned og = xb_add(&bar[XB_TOP], 1u);
;             const unsigned tg = og / nx;
;             if (og + 1u == (tg + 1u) * nx) xb_add(&bar[XB_TOPGEN], 1u);
;             else XB_SPIN(xb_ld(&bar[XB_TOPGEN]) == tg, bar);
;             __builtin_amdgcn_fence(__ATOMIC_ACQUIRE, "agent");
;             xb_add(&bar[XB_XGEN(b.x)], 1u);
;             asm volatile("s_waitcnt vmcnt(0)" ::: "memory");
;         } else {
;             XB_SPIN(xb_ld(&bar[XB_XGEN(b.x)]) == gen, bar);
;             __builtin_amdgcn_fence(__ATOMIC_ACQUIRE, "agent");
;             asm volatile("s_waitcnt vmcnt(0)" ::: "memory");
;         }
.LBB0_1653:
	s_waitcnt lgkmcnt(0)
	v_readfirstlane_b32 s8, v3
	v_readfirstlane_b32 s9, v1
	v_readlane_b32 s0, v252, 4
	s_lshl_b32 s0, s0, 8
	v_readlane_b32 s2, v252, 2
	v_readlane_b32 s3, v252, 3
	s_add_u32 s6, s2, s0
	s_addc_u32 s7, s3, 0
	s_mul_i32 s10, s8, 16
	s_mul_i32 s11, s9, 16
	v_mov_b32_e32 v4, 0x1000
	v_mov_b32_e32 v5, 1
	global_atomic_add v4, v4, v5, s[6:7] offset:1024 sc0
	v_mov_b32_e32 v1, 0x3400
	s_waitcnt vmcnt(0)
	v_readfirstlane_b32 s0, v4
	s_add_u32 s0, s0, 1
	s_cmp_lg_u32 s0, s10
	s_cbranch_scc1 .Lgbn_15
	buffer_wbl2 sc1
	buffer_inv sc1
	s_waitcnt vmcnt(0)
	global_atomic_add v1, v5, s[2:3]
	s_branch .Lgbw_15

; __device__ __forceinline__ unsigned xb_ld(unsigned* p)              { return __hip_atomic_load(p, __ATOMIC_RELAXED, __HIP_MEMORY_SCOPE_AGENT); }
; __device__ __forceinline__ unsigned xb_add(unsigned* p, unsigned v) { return __hip_atomic_fetch_add(p, v, __ATOMIC_RELAXED, __HIP_MEMORY_SCOPE_AGENT); }
; #define XB_SPIN(cond, bar) do { unsigned _sp = 0; while (cond) { __builtin_amdgcn_s_sleep(1); \
;     if ((++_sp & 255u) == 0u) { if (xb_ld(&(bar)[XB_TMO])) break; if (_sp > XB_SPIN_CAP) { atomicAdd(&(bar)[XB_TMO], 1u); break; } } } } while (0)
; __device__ __forceinline__ void xcd_barrier(const XcdBarrier& b) {
;     asm volatile("s_waitcnt vmcnt(0)" ::: "memory");
;     __syncthreads();
;     if (threadIdx.x == 0) {
;         unsigned* bar = b.bar;
;         __builtin_amdgcn_s_waitcnt(0);
;         unsigned nloc = b.st[0], nx = b.st[1];
;         if (nloc == 0u) { xcd_barrier_complete(bar, b.x, nloc, nx); b.st[0] = nloc; b.st[1] = nx; }
;         const unsigned old = xb_add(&bar[XB_XSUB(b.x)], 1u);
;         const unsigned gen = old / nloc;
;         if (old + 1u == (gen + 1u) * nloc) {
;             __builtin_amdgcn_fence(__ATOMIC_RELEASE, "agent");
;             asm volatile("s_waitcnt vmcnt(0)" ::: "memory");
;             const unsigned og = xb_add(&bar[XB_TOP], 1u);
;             const unsigned tg = og / nx;
;             if (og + 1u == (tg + 1u) * nx) xb_add(&bar[XB_TOPGEN], 1u);
;             else XB_SPIN(xb_ld(&bar[XB_TOPGEN]) == tg, bar);
;             __builtin_amdgcn_fence(__ATOMIC_ACQUIRE, "agent");
;             xb_add(&bar[XB_XGEN(b.x)], 1u);
;             asm volatile("s_waitcnt vmcnt(0)" ::: "memory");
;         } else {
;             XB_SPIN(xb_ld(&bar[XB_XGEN(b.x)]) == gen, bar);
;             __builtin_amdgcn_fence(__ATOMIC_ACQUIRE, "agent");
;             asm volatile("s_waitcnt vmcnt(0)" ::: "memory");
;         }
.LBB0_1721:
	s_waitcnt lgkmcnt(0)
	v_readfirstlane_b32 s8, v3
	v_readfirstlane_b32 s9, v1
	v_readlane_b32 s0, v252, 4
	s_lshl_b32 s0, s0, 8
	v_readlane_b32 s2, v252, 2
	v_readlane_b32 s3, v252, 3
	s_add_u32 s6, s2, s0
	s_addc_u32 s7, s3, 0
	s_mul_i32 s10, s8, 17
	s_mul_i32 s11, s9, 17
	v_mov_b32_e32 v4, 0x1000
	v_mov_b32_e32 v5, 1
	global_atomic_add v4, v4, v5, s[6:7] offset:1024 sc0
	v_mov_b32_e32 v1, 0x3400
	s_waitcnt vmcnt(0)
	v_readfirstlane_b32 s0, v4
	s_add_u32 s0, s0, 1
	s_cmp_lg_u32 s0, s10
	s_cbranch_scc1 .Lgbn_16
	buffer_wbl2 sc1
	buffer_inv sc1
	s_waitcnt vmcnt(0)
	global_atomic_add v1, v5, s[2:3]
	s_branch .Lgbw_16

; __device__ __forceinline__ unsigned xb_ld(unsigned* p)              { return __hip_atomic_load(p, __ATOMIC_RELAXED, __HIP_MEMORY_SCOPE_AGENT); }
; __device__ __forceinline__ unsigned xb_add(unsigned* p, unsigned v) { return __hip_atomic_fetch_add(p, v, __ATOMIC_RELAXED, __HIP_MEMORY_SCOPE_AGENT); }
; #define XB_SPIN(cond, bar) do { unsigned _sp = 0; while (cond) { __builtin_amdgcn_s_sleep(1); \
;     if ((++_sp & 255u) == 0u) { if (xb_ld(&(bar)[XB_TMO])) break; if (_sp > XB_SPIN_CAP) { atomicAdd(&(bar)[XB_TMO], 1u); break; } } } } while (0)
; __device__ __forceinline__ void xcd_barrier(const XcdBarrier& b) {
;     asm volatile("s_waitcnt vmcnt(0)" ::: "memory");
;     __syncthreads();
;     if (threadIdx.x == 0) {
;         unsigned* bar = b.bar;
;         __builtin_amdgcn_s_waitcnt(0);
;         unsigned nloc = b.st[0], nx = b.st[1];
;         if (nloc == 0u) { xcd_barrier_complete(bar, b.x, nloc, nx); b.st[0] = nloc; b.st[1] = nx; }
;         const unsigned old = xb_add(&bar[XB_XSUB(b.x)], 1u);
;         const unsigned gen = old / nloc;
;         if (old + 1u == (gen + 1u) * nloc) {
;             __builtin_amdgcn_fence(__ATOMIC_RELEASE, "agent");
;             asm volatile("s_waitcnt vmcnt(0)" ::: "memory");
;             const unsigned og = xb_add(&bar[XB_TOP], 1u);
;             const unsigned tg = og / nx;
;             if (og + 1u == (tg + 1u) * nx) xb_add(&bar[XB_TOPGEN], 1u);
;             else XB_SPIN(xb_ld(&bar[XB_TOPGEN]) == tg, bar);
;             __builtin_amdgcn_fence(__ATOMIC_ACQUIRE, "agent");
;             xb_add(&bar[XB_XGEN(b.x)], 1u);
;             asm volatile("s_waitcnt vmcnt(0)" ::: "memory");
;         } else {
;             XB_SPIN(xb_ld(&bar[XB_XGEN(b.x)]) == gen, bar);
;             __builtin_amdgcn_fence(__ATOMIC_ACQUIRE, "agent");
;             asm volatile("s_waitcnt vmcnt(0)" ::: "memory");
;         }
.LBB0_1855:
	s_waitcnt lgkmcnt(0)
	v_readfirstlane_b32 s8, v3
	v_readfirstlane_b32 s9, v1
	v_readlane_b32 s0, v252, 4
	s_lshl_b32 s0, s0, 8
	v_readlane_b32 s2, v252, 2
	v_readlane_b32 s3, v252, 3
	s_add_u32 s6, s2, s0
	s_addc_u32 s7, s3, 0
	s_mul_i32 s10, s8, 18
	s_mul_i32 s11, s9, 18
	v_mov_b32_e32 v4, 0x1000
	v_mov_b32_e32 v5, 1
	global_atomic_add v4, v4, v5, s[6:7] offset:1024 sc0
	v_mov_b32_e32 v1, 0x3400
	s_waitcnt vmcnt(0)
	v_readfirstlane_b32 s0, v4
	s_add_u32 s0, s0, 1
	s_cmp_lg_u32 s0, s10
	s_cbranch_scc1 .Lgbn_17
	buffer_wbl2 sc1
	buffer_inv sc1
	s_waitcnt vmcnt(0)
	global_atomic_add v1, v5, s[2:3]
	s_branch .Lgbw_17

; __device__ __forceinline__ unsigned xb_ld(unsigned* p)              { return __hip_atomic_load(p, __ATOMIC_RELAXED, __HIP_MEMORY_SCOPE_AGENT); }
; __device__ __forceinline__ unsigned xb_add(unsigned* p, unsigned v) { return __hip_atomic_fetch_add(p, v, __ATOMIC_RELAXED, __HIP_MEMORY_SCOPE_AGENT); }
; #define XB_SPIN(cond, bar) do { unsigned _sp = 0; while (cond) { __builtin_amdgcn_s_sleep(1); \
;     if ((++_sp & 255u) == 0u) { if (xb_ld(&(bar)[XB_TMO])) break; if (_sp > XB_SPIN_CAP) { atomicAdd(&(bar)[XB_TMO], 1u); break; } } } } while (0)
; __device__ __forceinline__ void xcd_barrier(const XcdBarrier& b) {
;     asm volatile("s_waitcnt vmcnt(0)" ::: "memory");
;     __syncthreads();
;     if (threadIdx.x == 0) {
;         unsigned* bar = b.bar;
;         __builtin_amdgcn_s_waitcnt(0);
;         unsigned nloc = b.st[0], nx = b.st[1];
;         if (nloc == 0u) { xcd_barrier_complete(bar, b.x, nloc, nx); b.st[0] = nloc; b.st[1] = nx; }
;         const unsigned old = xb_add(&bar[XB_XSUB(b.x)], 1u);
;         const unsigned gen = old / nloc;
;         if (old + 1u == (gen + 1u) * nloc) {
;             __builtin_amdgcn_fence(__ATOMIC_RELEASE, "agent");
;             asm volatile("s_waitcnt vmcnt(0)" ::: "memory");
;             const unsigned og = xb_add(&bar[XB_TOP], 1u);
;             const unsigned tg = og / nx;
;             if (og + 1u == (tg + 1u) * nx) xb_add(&bar[XB_TOPGEN], 1u);
;             else XB_SPIN(xb_ld(&bar[XB_TOPGEN]) == tg, bar);
;             __builtin_amdgcn_fence(__ATOMIC_ACQUIRE, "agent");
;             xb_add(&bar[XB_XGEN(b.x)], 1u);
;             asm volatile("s_waitcnt vmcnt(0)" ::: "memory");
;         } else {
;             XB_SPIN(xb_ld(&bar[XB_XGEN(b.x)]) == gen, bar);
;             __builtin_amdgcn_fence(__ATOMIC_ACQUIRE, "agent");
;             asm volatile("s_waitcnt vmcnt(0)" ::: "memory");
;         }
.LBB0_1999:
	s_waitcnt lgkmcnt(0)
	v_readfirstlane_b32 s8, v3
	v_readfirstlane_b32 s9, v1
	v_readlane_b32 s0, v252, 4
	s_lshl_b32 s0, s0, 8
	v_readlane_b32 s2, v252, 2
	v_readlane_b32 s3, v252, 3
	s_add_u32 s6, s2, s0
	s_addc_u32 s7, s3, 0
	s_mul_i32 s10, s8, 19
	s_mul_i32 s11, s9, 19
	v_mov_b32_e32 v4, 0x1000
	v_mov_b32_e32 v5, 1
	global_atomic_add v4, v4, v5, s[6:7] offset:1024 sc0
	v_mov_b32_e32 v1, 0x3400
	s_waitcnt vmcnt(0)
	v_readfirstlane_b32 s0, v4
	s_add_u32 s0, s0, 1
	s_cmp_lg_u32 s0, s10
	s_cbranch_scc1 .Lgbn_18
	buffer_wbl2 sc1
	buffer_inv sc1
	s_waitcnt vmcnt(0)
	global_atomic_add v1, v5, s[2:3]
	s_branch .Lgbw_18
